# mixer work queues: after draining its own queue a workgroup reads all eight queue heads once and skips the fetch-and-add round trip on queues already exhausted
# baseline (speedup 1.0000x reference)
.LBB0_608:
	s_or_b64 exec, exec, s[4:5]
	s_mov_b64 s[66:67], s[96:97]
	s_waitcnt lgkmcnt(0)
	s_barrier
	s_mov_b32 s101, 0
	s_load_dwordx2 s[68:69], s[66:67], 0xe0
	v_readlane_b32 s4, v254, 26
	v_readlane_b32 s5, v254, 27
	s_and_b64 s[4:5], s[4:5], exec
	s_movk_i32 s1, 0xa8
	s_cselect_b32 s65, s1, 0xdc
	s_lshl_b32 s22, s44, 9
	s_lshl_b64 s[4:5], s[22:23], 2
	s_waitcnt lgkmcnt(0)
	s_add_u32 s1, s68, s4
	s_addc_u32 s2, s69, s5
	s_add_u32 s70, s1, 0x8100
	s_addc_u32 s71, s2, 0
	s_lshl_b32 s22, s44, 5
	s_lshl_b64 s[4:5], s[22:23], 2
	s_add_u32 s1, s68, s4
	s_addc_u32 s2, s69, s5
	s_add_u32 s72, s1, 0xe000
	s_addc_u32 s73, s2, 0
	s_add_u32 s74, s68, 0x38028000
	s_addc_u32 s75, s69, 0
	s_add_u32 s1, s68, 0x3d868000
	v_writelane_b32 v254, s1, 32
	s_addc_u32 s1, s69, 0
	s_add_u32 s76, s68, 0x38038000
	s_addc_u32 s77, s69, 0
	s_add_u32 s4, s68, 0x38028080
	v_writelane_b32 v254, s1, 33
	s_addc_u32 s5, s69, 0
	v_writelane_b32 v254, s4, 34
	s_add_u32 s1, s68, 0x5c068000
	s_addc_u32 s79, s69, 0
	v_writelane_b32 v254, s5, 35
	v_writelane_b32 v254, s1, 36
	s_add_u32 s1, s68, 0x5e468000
	v_writelane_b32 v254, s1, 37
	s_mul_hi_u32 s1, s44, 0x2400
	s_addc_u32 s63, s69, 0
	v_writelane_b32 v254, s1, 12
	s_mul_i32 s1, s44, 0x2400
	s_add_u32 s78, s68, 0x5ed68000
	v_writelane_b32 v254, s1, 10
	s_mul_hi_u32 s1, s44, 0xc00
	s_addc_u32 s62, s69, 0
	s_lshl_b64 s[4:5], s[44:45], 19
	v_writelane_b32 v254, s1, 14
	s_mul_i32 s1, s44, 0xc00
	s_lshl_b64 s[80:81], s[44:45], 11
	v_writelane_b32 v254, s1, 5
	s_add_u32 s1, s68, 0x5bc68000
	v_writelane_b32 v254, s1, 38
	s_addc_u32 s1, s69, 0
	v_writelane_b32 v254, s1, 39
	s_add_u32 s1, s68, 0x37028000
	v_writelane_b32 v254, s1, 40
	s_addc_u32 s1, s69, 0
	s_mov_b64 s[6:7], s[44:45]
	s_add_u32 s45, s68, 0x3c868000
	s_addc_u32 s97, s69, 0
	s_lshl_b64 s[6:7], s[6:7], 22
	s_add_u32 s46, s68, 0x59c68000
	s_addc_u32 s47, s69, 0
	s_add_u32 s50, s68, 0x59668000
	s_addc_u32 s51, s69, 0
	v_writelane_b32 v254, s1, 41
	s_add_u32 s1, s68, s4
	s_addc_u32 s2, s69, s5
	s_add_u32 s1, s1, 0x36e28000
	v_writelane_b32 v254, s1, 42
	s_addc_u32 s1, s2, 0
	s_add_u32 s53, s68, 0x5ed68400
	s_addc_u32 s2, s69, 0
	s_add_u32 s58, s68, 0x56668000
	s_addc_u32 s59, s69, 0
	v_writelane_b32 v254, s1, 43
	s_add_u32 s1, s68, s6
	s_addc_u32 s4, s69, s7
	s_add_u32 s34, s1, 0x35e28000
	s_getreg_b32 s96, hwreg(HW_REG_XCC_ID, 0, 4)
	s_addc_u32 s35, s4, 0
	s_mov_b32 s36, 0
	s_branch .LBB0_610

.LBB0_610:
	s_add_i32 s1, s36, s96
	s_and_b32 s1, s1, 7
	s_lshl_b32 s10, s1, 6
	s_barrier
	s_and_saveexec_b64 s[4:5], s[20:21]
	s_cbranch_execz .LBB0_614
	s_cmp_lg_u32 s36, 1
	s_cbranch_scc1 .Lmy_q_nom
	s_mov_b64 s[8:9], exec
	s_mov_b64 exec, 0xff
	v_mbcnt_lo_u32_b32 v3, -1, 0
	v_lshlrev_b32_e32 v3, 8, v3
	global_load_dword v3, v3, s[70:71] sc1
	s_waitcnt vmcnt(0)
	v_cmp_le_u32_e32 vcc, s65, v3
	s_nop 3
	s_and_b32 s100, vcc_lo, 0xff
	s_mov_b64 exec, s[8:9]
.Lmy_q_nom:
	s_cmp_eq_u32 s36, 0
	s_cbranch_scc1 .Lmy_q_do
	s_bitcmp1_b32 s100, s1
	s_cbranch_scc0 .Lmy_q_do
	v_mov_b32_e32 v3, s95
	v_mov_b32_e32 v2, s65
	ds_write_b32 v3, v2
	s_branch .LBB0_614
.Lmy_q_do:
	s_mov_b64 s[8:9], exec
	v_mbcnt_lo_u32_b32 v2, s8, 0
	v_mbcnt_hi_u32_b32 v2, s9, v2
	v_cmp_eq_u32_e32 vcc, 0, v2
	s_and_saveexec_b64 s[6:7], vcc
	s_cbranch_execz .LBB0_613
	s_lshl_b32 s11, s10, 2
	s_bcnt1_i32_b64 s8, s[8:9]
	v_mov_b32_e32 v3, s11
	v_mov_b32_e32 v4, s8
	global_atomic_add v3, v3, v4, s[70:71] sc0

.LBB0_639:
	s_and_b64 vcc, exec, s[4:5]
	s_cbranch_vccz .LBB0_666
	s_cmp_lg_u32 s101, 0
	s_cbranch_scc0 .Lnegc_calc_a
	v_mov_b32_e32 v50, v0
	s_nop 0
	v_readfirstlane_b32 s10, v50
	s_mov_b32 s11, s101
	s_ashr_i32 s1, s10, 6
	s_cmp_lt_i32 s1, 4
	s_branch .Lnegc_done_a
.Lnegc_calc_a:
	v_mov_b32_e32 v2, v0
	s_load_dwordx4 s[4:7], s[66:67], 0x48
	v_readlane_b32 s10, v254, 30
	v_and_b32_e32 v6, 64, v177
	v_add_u32_e32 v6, 64, v6
	v_and_or_b32 v130, v2, 63, s10
	v_lshlrev_b64 v[2:3], 2, v[130:131]
	s_waitcnt lgkmcnt(0)
	v_lshl_add_u64 v[4:5], s[4:5], 0, v[2:3]
	v_lshl_add_u64 v[2:3], s[6:7], 0, v[2:3]
	global_load_dword v2, v[2:3], off
	v_xor_b32_e32 v7, 32, v177
	global_load_dword v4, v[4:5], off
	v_cmp_lt_i32_e32 vcc, v7, v6
	v_mov_b32_e32 v50, v0
	v_readlane_b32 s11, v254, 31
	v_cndmask_b32_e32 v7, v177, v7, vcc
	v_lshlrev_b32_e32 v7, 2, v7
	v_readfirstlane_b32 s10, v50
	s_ashr_i32 s1, s10, 6
	s_cmp_lt_i32 s1, 4
	s_waitcnt vmcnt(0)
	v_and_b32_e32 v3, 0x7fffffff, v2
	ds_bpermute_b32 v3, v7, v3
	v_and_b32_e32 v5, 0x7fffffff, v4
	ds_bpermute_b32 v5, v7, v5
	v_max_f32_e64 v2, |v2|, |v2|
	v_max_f32_e64 v4, |v4|, |v4|
	s_waitcnt lgkmcnt(1)
	v_max_f32_e32 v3, v3, v3
	v_max_f32_e32 v2, v2, v3
	v_xor_b32_e32 v3, 16, v177
	v_cmp_lt_i32_e32 vcc, v3, v6
	s_waitcnt lgkmcnt(0)
	v_max_f32_e32 v5, v5, v5
	v_max_f32_e32 v4, v4, v5
	v_cndmask_b32_e32 v3, v177, v3, vcc
	v_lshlrev_b32_e32 v3, 2, v3
	ds_bpermute_b32 v5, v3, v4
	ds_bpermute_b32 v3, v3, v2
	s_waitcnt lgkmcnt(1)
	v_max_f32_e32 v5, v5, v5
	s_waitcnt lgkmcnt(0)
	v_max_f32_e32 v3, v3, v3
	v_max_f32_e32 v2, v2, v3
	v_xor_b32_e32 v3, 8, v177
	v_cmp_lt_i32_e32 vcc, v3, v6
	v_max_f32_e32 v4, v4, v5
	s_nop 0
	v_cndmask_b32_e32 v3, v177, v3, vcc
	v_lshlrev_b32_e32 v3, 2, v3
	ds_bpermute_b32 v5, v3, v4
	ds_bpermute_b32 v3, v3, v2
	s_waitcnt lgkmcnt(1)
	v_max_f32_e32 v5, v5, v5
	s_waitcnt lgkmcnt(0)
	v_max_f32_e32 v3, v3, v3
	v_max_f32_e32 v2, v2, v3
	v_xor_b32_e32 v3, 4, v177
	v_cmp_lt_i32_e32 vcc, v3, v6
	v_max_f32_e32 v4, v4, v5
	s_nop 0
	v_cndmask_b32_e32 v3, v177, v3, vcc
	v_lshlrev_b32_e32 v3, 2, v3
	ds_bpermute_b32 v5, v3, v4
	ds_bpermute_b32 v3, v3, v2
	s_waitcnt lgkmcnt(1)
	v_max_f32_e32 v5, v5, v5
	s_waitcnt lgkmcnt(0)
	v_max_f32_e32 v3, v3, v3
	v_max_f32_e32 v2, v2, v3
	v_xor_b32_e32 v3, 2, v177
	v_cmp_lt_i32_e32 vcc, v3, v6
	v_max_f32_e32 v4, v4, v5
	s_nop 0
	v_cndmask_b32_e32 v3, v177, v3, vcc
	v_lshlrev_b32_e32 v3, 2, v3
	ds_bpermute_b32 v5, v3, v4
	ds_bpermute_b32 v3, v3, v2
	s_waitcnt lgkmcnt(1)
	v_max_f32_e32 v5, v5, v5
	s_waitcnt lgkmcnt(0)
	v_max_f32_e32 v3, v3, v3
	v_max_f32_e32 v2, v2, v3
	v_xor_b32_e32 v3, 1, v177
	v_cmp_lt_i32_e32 vcc, v3, v6
	v_max_f32_e32 v4, v4, v5
	s_nop 0
	v_cndmask_b32_e32 v3, v177, v3, vcc
	v_lshlrev_b32_e32 v3, 2, v3
	ds_bpermute_b32 v5, v3, v4
	ds_bpermute_b32 v3, v3, v2
	s_waitcnt lgkmcnt(1)
	v_max_f32_e32 v5, v5, v5
	v_max_f32_e32 v4, v4, v5
	s_waitcnt lgkmcnt(0)
	v_max_f32_e32 v3, v3, v3
	v_max_f32_e32 v2, v2, v3
	v_mul_f32_e32 v3, 0xc13c5bb7, v4
	v_mul_f32_e32 v2, v2, v3
	s_nop 0
	v_readfirstlane_b32 s11, v2
	s_nop 0
	s_mov_b32 s101, s11
.Lnegc_done_a:
	s_cbranch_scc1 .LBB0_642
	s_setprio 1

.LBB0_689:
	s_andn2_b64 vcc, exec, s[4:5]
	s_cbranch_vccnz .LBB0_697
	s_cmp_lg_u32 s101, 0
	s_cbranch_scc0 .Lnegc_calc_b
	v_mov_b32_e32 v50, v0
	s_nop 0
	v_readfirstlane_b32 s11, v50
	s_mov_b32 s13, s101
	s_ashr_i32 s1, s11, 6
	s_cmp_lt_i32 s1, 4
	s_branch .Lnegc_done_b
.Lnegc_calc_b:
	v_mov_b32_e32 v2, v0
	s_load_dwordx4 s[4:7], s[66:67], 0x48
	v_readlane_b32 s10, v254, 30
	v_and_b32_e32 v6, 64, v177
	v_add_u32_e32 v6, 64, v6
	v_and_or_b32 v130, v2, 63, s10
	v_lshlrev_b64 v[2:3], 2, v[130:131]
	s_waitcnt lgkmcnt(0)
	v_lshl_add_u64 v[4:5], s[4:5], 0, v[2:3]
	v_lshl_add_u64 v[2:3], s[6:7], 0, v[2:3]
	global_load_dword v2, v[2:3], off
	v_xor_b32_e32 v7, 32, v177
	global_load_dword v4, v[4:5], off
	v_cmp_lt_i32_e32 vcc, v7, v6
	v_readlane_b32 s11, v254, 31
	v_mov_b32_e32 v50, v0
	v_cndmask_b32_e32 v7, v177, v7, vcc
	v_lshlrev_b32_e32 v7, 2, v7
	s_waitcnt vmcnt(0)
	v_and_b32_e32 v3, 0x7fffffff, v2
	ds_bpermute_b32 v3, v7, v3
	v_and_b32_e32 v5, 0x7fffffff, v4
	ds_bpermute_b32 v5, v7, v5
	v_max_f32_e64 v2, |v2|, |v2|
	v_max_f32_e64 v4, |v4|, |v4|
	s_waitcnt lgkmcnt(1)
	v_max_f32_e32 v3, v3, v3
	v_max_f32_e32 v2, v2, v3
	v_xor_b32_e32 v3, 16, v177
	v_cmp_lt_i32_e32 vcc, v3, v6
	s_waitcnt lgkmcnt(0)
	v_max_f32_e32 v5, v5, v5
	v_max_f32_e32 v4, v4, v5
	v_cndmask_b32_e32 v3, v177, v3, vcc
	v_lshlrev_b32_e32 v3, 2, v3
	ds_bpermute_b32 v5, v3, v4
	ds_bpermute_b32 v3, v3, v2
	v_readfirstlane_b32 s11, v50
	s_ashr_i32 s1, s11, 6
	s_cmp_lt_i32 s1, 4
	s_waitcnt lgkmcnt(1)
	v_max_f32_e32 v5, v5, v5
	s_waitcnt lgkmcnt(0)
	v_max_f32_e32 v3, v3, v3
	v_max_f32_e32 v2, v2, v3
	v_xor_b32_e32 v3, 8, v177
	v_cmp_lt_i32_e32 vcc, v3, v6
	v_max_f32_e32 v4, v4, v5
	s_nop 0
	v_cndmask_b32_e32 v3, v177, v3, vcc
	v_lshlrev_b32_e32 v3, 2, v3
	ds_bpermute_b32 v5, v3, v4
	ds_bpermute_b32 v3, v3, v2
	s_waitcnt lgkmcnt(1)
	v_max_f32_e32 v5, v5, v5
	s_waitcnt lgkmcnt(0)
	v_max_f32_e32 v3, v3, v3
	v_max_f32_e32 v2, v2, v3
	v_xor_b32_e32 v3, 4, v177
	v_cmp_lt_i32_e32 vcc, v3, v6
	v_max_f32_e32 v4, v4, v5
	s_nop 0
	v_cndmask_b32_e32 v3, v177, v3, vcc
	v_lshlrev_b32_e32 v3, 2, v3
	ds_bpermute_b32 v5, v3, v4
	ds_bpermute_b32 v3, v3, v2
	s_waitcnt lgkmcnt(1)
	v_max_f32_e32 v5, v5, v5
	s_waitcnt lgkmcnt(0)
	v_max_f32_e32 v3, v3, v3
	v_max_f32_e32 v2, v2, v3
	v_xor_b32_e32 v3, 2, v177
	v_cmp_lt_i32_e32 vcc, v3, v6
	v_max_f32_e32 v4, v4, v5
	s_nop 0
	v_cndmask_b32_e32 v3, v177, v3, vcc
	v_lshlrev_b32_e32 v3, 2, v3
	ds_bpermute_b32 v5, v3, v4
	ds_bpermute_b32 v3, v3, v2
	s_waitcnt lgkmcnt(1)
	v_max_f32_e32 v5, v5, v5
	s_waitcnt lgkmcnt(0)
	v_max_f32_e32 v3, v3, v3
	v_max_f32_e32 v2, v2, v3
	v_xor_b32_e32 v3, 1, v177
	v_cmp_lt_i32_e32 vcc, v3, v6
	v_max_f32_e32 v4, v4, v5
	s_nop 0
	v_cndmask_b32_e32 v3, v177, v3, vcc
	v_lshlrev_b32_e32 v3, 2, v3
	ds_bpermute_b32 v5, v3, v4
	ds_bpermute_b32 v3, v3, v2
	s_waitcnt lgkmcnt(1)
	v_max_f32_e32 v5, v5, v5
	v_max_f32_e32 v4, v4, v5
	s_waitcnt lgkmcnt(0)
	v_max_f32_e32 v3, v3, v3
	v_max_f32_e32 v2, v2, v3
	v_mul_f32_e32 v3, 0xc13c5bb7, v4
	v_mul_f32_e32 v2, v2, v3
	s_nop 0
	v_readfirstlane_b32 s13, v2
	s_nop 0
	s_mov_b32 s101, s13
.Lnegc_done_b:
	s_cbranch_scc1 .LBB0_692
	s_setprio 1
